# post-projection per-token tail: the 7 independent loads (K copy x3, V row, indexer-k, norm gamma/beta) issued together with one wait instead of a load-wait-store ladder
# speedup vs baseline: 1.0107x; 1.0028x over previous
.LBB0_324:
	s_or_b64 exec, exec, s[72:73]
	v_lshl_add_u64 v[36:37], s[50:51], 0, v[22:23]
	v_add_co_u32_e32 v38, vcc, 0x37cd0000, v36
	v_mov_b32_e32 v45, 0
	s_nop 0
	v_addc_co_u32_e32 v39, vcc, 0, v37, vcc
	v_lshl_add_u64 v[40:41], s[50:51], 0, v[10:11]
	v_add_co_u32_e32 v40, vcc, 0x4d6d0000, v40
	v_lshl_add_u64 v[42:43], s[50:51], 0, v[20:21]
	s_nop 0
	v_addc_co_u32_e32 v41, vcc, 0, v41, vcc
	v_add_co_u32_e32 v36, vcc, s15, v36
	v_mov_b32_e32 v46, 0
	s_nop 0
	v_addc_co_u32_e32 v37, vcc, 0, v37, vcc
	global_load_ushort v238, v[38:39], off offset:2112
	global_load_ushort v240, v[38:39], off offset:2432
	global_load_ushort v239, v[42:43], off
	v_lshl_add_u64 v[244:245], s[50:51], 0, v[18:19]
	global_load_dwordx2 v[246:247], v[244:245], off
	global_load_ushort v241, v[36:37], off offset:1024
	global_load_dword v248, v[2:3], off
	global_load_dword v249, v[4:5], off
	v_mov_b32_e32 v47, 0
	v_mov_b32_e32 v48, 0
	v_mov_b32_e32 v49, 0
	v_mov_b32_e32 v50, 0
	s_add_i32 s14, s14, s16
	s_add_u32 s0, s0, s18
	s_addc_u32 s1, s1, s19
	v_lshl_add_u64 v[6:7], v[6:7], 0, s[20:21]
	v_lshl_add_u64 v[10:11], v[10:11], 0, s[20:21]
	v_lshl_add_u64 v[16:17], v[16:17], 0, s[52:53]
	v_lshl_add_u64 v[20:21], v[20:21], 0, s[52:53]
	v_lshl_add_u64 v[22:23], v[22:23], 0, s[52:53]
	v_lshl_add_u64 v[24:25], v[24:25], 0, s[52:53]
	s_cmpk_gt_i32 s14, 0x3fff
	v_lshl_add_u64 v[26:27], v[26:27], 0, s[52:53]
	s_waitcnt vmcnt(0)
	v_lshlrev_b32_e32 v44, 16, v238
	v_cvt_pk_fp8_f32 v45, v44, v44
	v_mov_b32_e32 v44, 0
	global_store_byte v[40:41], v45, off offset:32
	v_mov_b32_e32 v45, 0
	v_lshlrev_b32_e32 v42, 16, v239
	v_cvt_pk_fp8_f32 v44, v42, v42
	v_lshl_add_u64 v[42:43], s[50:51], 0, v[12:13]
	v_lshl_add_u64 v[12:13], v[12:13], 0, s[20:21]
	global_store_byte v[42:43], v44, off
	v_mov_b32_e32 v42, 0
	v_lshlrev_b32_e32 v38, 16, v240
	v_cvt_pk_fp8_f32 v42, v38, v38
	v_lshl_add_u64 v[38:39], s[50:51], 0, v[18:19]
	v_lshl_add_u64 v[18:19], v[18:19], 0, s[52:53]
	global_store_byte v[40:41], v42, off offset:192
	s_nop 0
	v_lshl_add_u64 v[36:37], s[50:51], 0, v[8:9]
	v_lshl_add_u64 v[40:41], s[50:51], 0, v[14:15]
	v_lshl_add_u64 v[8:9], v[8:9], 0, s[20:21]
	v_lshl_add_u64 v[14:15], v[14:15], 0, s[26:27]
	v_lshlrev_b32_e32 v42, 16, v241
	v_lshlrev_b32_e32 v51, 16, v246
	v_and_b32_e32 v38, 0xffff0000, v246
	v_cvt_pk_fp8_f32 v45, v51, v38
	s_nop 0
	v_add_f32_dpp v38, v42, v42 row_shr:1 row_mask:0xf bank_mask:0xf bound_ctrl:1
	s_nop 1
	v_add_f32_dpp v38, v38, v38 row_shr:2 row_mask:0xf bank_mask:0xf bound_ctrl:1
	s_nop 1
	v_add_f32_dpp v38, v38, v38 row_shr:4 row_mask:0xf bank_mask:0xf bound_ctrl:1
	s_nop 1
	v_add_f32_dpp v38, v38, v38 row_shr:8 row_mask:0xf bank_mask:0xf bound_ctrl:1
	s_nop 1
	v_mov_b32_dpp v46, v38 row_bcast:15 row_mask:0xa bank_mask:0xf
	v_add_f32_e32 v38, v38, v46
	s_nop 1
	v_mov_b32_dpp v47, v38 row_bcast:31 row_mask:0xc bank_mask:0xf
	v_add_f32_e32 v38, v38, v47
	s_nop 0
	v_readlane_b32 s29, v38, 63
	s_nop 1
	v_fmac_f32_e32 v42, s29, v32
	v_mul_f32_e32 v38, v42, v42
	s_nop 1
	v_mov_b32_dpp v48, v38 row_shr:1 row_mask:0xf bank_mask:0xf
	v_fmac_f32_e32 v48, v42, v42
	s_nop 1
	v_add_f32_dpp v38, v48, v48 row_shr:2 row_mask:0xf bank_mask:0xf bound_ctrl:1
	s_nop 1
	v_add_f32_dpp v38, v38, v38 row_shr:4 row_mask:0xf bank_mask:0xf bound_ctrl:1
	s_nop 1
	v_add_f32_dpp v38, v38, v38 row_shr:8 row_mask:0xf bank_mask:0xf bound_ctrl:1
	s_nop 1
	v_mov_b32_dpp v49, v38 row_bcast:15 row_mask:0xa bank_mask:0xf
	v_add_f32_e32 v38, v38, v49
	s_nop 1
	v_mov_b32_dpp v50, v38 row_bcast:31 row_mask:0xc bank_mask:0xf
	v_add_f32_e32 v38, v38, v50
	s_nop 0
	v_readlane_b32 s29, v38, 63
	s_nop 1
	v_fma_f32 v38, s29, v33, v31
	v_mul_f32_e32 v46, 0x4b800000, v38
	v_cmp_gt_f32_e32 vcc, s17, v38
	s_nop 1
	v_cndmask_b32_e32 v38, v38, v46, vcc
	v_rsq_f32_e32 v38, v38
	v_lshlrev_b32_e32 v46, 16, v247
	v_and_b32_e32 v39, 0xffff0000, v247
	v_cvt_pk_fp8_f32 v45, v46, v39 op_sel:[0,0,1]
	v_mul_f32_e32 v39, 0x45800000, v38
	v_cndmask_b32_e32 v38, v38, v39, vcc
	v_mul_f32_e32 v38, v42, v38
	v_fma_f32 v44, v248, v38, v249
	ds_bpermute_b32 v38, v29, v44
	v_mul_f32_e32 v35, v35, v44
	global_store_dword v[36:37], v45, off
	s_waitcnt lgkmcnt(0)
	v_fma_f32 v36, -v34, v38, v35
	v_fmac_f32_e32 v35, v34, v38
	v_cndmask_b32_e64 v34, v44, v35, s[10:11]
	v_cndmask_b32_e64 v34, v34, v36, s[8:9]
	v_bfe_u32 v35, v34, 16, 1
	v_add3_u32 v34, v34, v35, s3
	global_store_short_d16_hi v[40:41], v34, off
	s_cbranch_scc1 .LBB0_327
